# code placement: one cold 4-byte pad at the down-GEMM phase entry so its K-loop MFMA/ds_read runs start 8-byte aligned (as in the baseline)
# baseline (speedup 1.0000x reference)
.LBB0_2033:
	s_nop 0
	s_cmp_lt_i32 s94, 8
	s_cselect_b64 s[0:1], -1, 0
	s_cmp_gt_i32 s95, 7
	s_cselect_b64 s[2:3], -1, 0
	s_and_b64 s[0:1], s[0:1], s[2:3]
	s_andn2_b64 vcc, exec, s[0:1]
	s_cbranch_vccnz .LBB0_2189
	s_add_u32 s3, s74, 0x20000000
	s_addc_u32 s34, s75, 0
	s_add_u32 s35, s74, 0x9000000
	s_addc_u32 s54, s75, 0
	s_add_u32 s55, s74, 0x1fa00000
	s_addc_u32 s56, s75, 0
	s_add_u32 s10, s74, 0x29000000
	s_addc_u32 s11, s75, 0
	s_add_i32 s0, 0, 0x202c0
	v_mov_b32_e32 v1, s0
	ds_read_b32 v1, v1
	s_and_b64 vcc, exec, s[24:25]
	s_mov_b64 s[0:1], -1
	s_waitcnt lgkmcnt(0)
	v_readfirstlane_b32 s57, v1
	s_cbranch_vccnz .LBB0_2101
	s_and_b32 s0, s93, 7
	s_mul_i32 s0, s57, s0
	s_ashr_i32 s1, s0, 31
	s_lshr_b32 s1, s1, 29
	s_add_i32 s1, s0, s1
	s_add_i32 s0, s0, s57
	s_ashr_i32 s30, s1, 3
	s_ashr_i32 s1, s0, 31
	s_lshr_b32 s1, s1, 29
	s_add_i32 s0, s0, s1
	s_ashr_i32 s0, s0, 3
	s_sub_i32 s31, s0, s30
	s_lshl_b32 s2, s31, 3
	s_ashr_i32 s4, s93, 3
	s_sub_i32 s20, s2, s4
	s_add_i32 s20, s20, 31
	s_lshl_b32 s58, s31, 2
	s_and_b32 s5, s20, 0xffffffe0
	s_cmp_gt_i32 s2, s4
	s_cselect_b64 s[6:7], -1, 0
	s_and_b64 s[0:1], s[6:7], exec
	s_cselect_b32 s0, s5, 0
	s_sub_i32 s59, s4, s2
	s_add_i32 s2, s0, s59
	s_cmp_gt_i32 s2, -1
	s_cselect_b64 s[0:1], -1, 0
	s_cmp_lt_i32 s2, s58
	s_cselect_b64 s[4:5], -1, 0
	s_and_b64 s[4:5], s[0:1], s[4:5]
	v_cndmask_b32_e64 v1, 0, 1, s[4:5]
	v_cmp_ne_u32_e64 s[0:1], 1, v1
	s_andn2_b64 vcc, exec, s[4:5]
	v_readfirstlane_b32 s21, v0
	s_cbranch_vccnz .LBB0_2037
	s_lshr_b32 s2, s2, 2
	s_and_b32 s2, s2, 0x1ffffffc
	s_sub_i32 s4, s31, s2
	s_min_i32 s4, s4, 4
	s_abs_i32 s5, s4
	v_cvt_f32_u32_e32 v1, s5
	s_sub_i32 s12, 0, s5
	s_and_b32 s8, s59, 15
	s_add_i32 s2, s2, s30
	v_rcp_iflag_f32_e32 v1, v1
	s_ashr_i32 s9, s4, 31
	v_mul_f32_e32 v1, 0x4f7ffffe, v1
	v_cvt_u32_f32_e32 v1, v1
	s_nop 0
	v_readfirstlane_b32 s13, v1
	s_mul_i32 s12, s12, s13
	s_mul_hi_u32 s12, s13, s12
	s_add_i32 s13, s13, s12
	s_mul_hi_u32 s12, s8, s13
	s_mul_i32 s13, s12, s5
	s_sub_i32 s13, s8, s13
	s_add_i32 s14, s12, 1
	s_sub_i32 s15, s13, s5
	s_cmp_ge_u32 s13, s5
	s_cselect_b32 s12, s14, s12
	s_cselect_b32 s13, s15, s13
	s_add_i32 s14, s12, 1
	s_cmp_ge_u32 s13, s5
	s_cselect_b32 s5, s14, s12
	s_xor_b32 s5, s5, s9
	s_sub_i32 s38, s5, s9
	s_mul_i32 s4, s38, s4
	s_sub_i32 s4, s8, s4
	s_add_i32 s22, s2, s4
